# nt hint also on the remaining wide loads of P0a (weight abs-max / conversion streams)
# speedup vs baseline: 1.0097x; 1.0097x over previous
.LBB0_13:
	s_mul_hi_i32 s6, s5, 0xb81702e1
	s_add_i32 s6, s6, s5
	s_lshr_b32 s7, s6, 31
	s_ashr_i32 s22, s6, 6
	s_add_i32 s22, s22, s7
	s_mul_i32 s6, s22, 0xffffe9c0
	v_add_u32_e32 v2, s6, v1
	v_cmp_gt_i32_e64 s[6:7], s3, v2
	v_mov_b32_e32 v10, 0
	v_ashrrev_i32_e32 v3, 31, v2
	v_mov_b32_e32 v9, 0
	v_mov_b32_e32 v8, 0
	v_mov_b32_e32 v7, 0
	s_and_saveexec_b64 s[8:9], s[6:7]
	s_cbranch_execz .LBB0_15
	v_lshl_add_u32 v7, s22, 8, v4
	v_lshl_add_u64 v[32:33], v[2:3], 2, s[10:11]
	v_mad_i64_i32 v[16:17], s[22:23], v7, s4, v[32:33]
	v_or_b32_e32 v8, 1, v7
	v_mad_i64_i32 v[18:19], s[22:23], v8, s4, v[32:33]
	s_waitcnt lgkmcnt(3)
	global_load_dwordx4 v[8:11], v[16:17], off nt
	s_waitcnt lgkmcnt(0)
	global_load_dwordx4 v[12:15], v[18:19], off nt
	v_or_b32_e32 v16, 2, v7
	v_mad_i64_i32 v[24:25], s[22:23], v16, s4, v[32:33]
	v_or_b32_e32 v16, 3, v7
	v_mad_i64_i32 v[26:27], s[22:23], v16, s4, v[32:33]
	global_load_dwordx4 v[16:19], v[24:25], off nt
	global_load_dwordx4 v[20:23], v[26:27], off nt
	v_or_b32_e32 v24, 4, v7
	v_mad_i64_i32 v[34:35], s[22:23], v24, s4, v[32:33]
	v_or_b32_e32 v24, 5, v7
	v_mad_i64_i32 v[36:37], s[22:23], v24, s4, v[32:33]
	global_load_dwordx4 v[24:27], v[34:35], off nt
	global_load_dwordx4 v[28:31], v[36:37], off nt
	v_or_b32_e32 v34, 6, v7
	v_mad_i64_i32 v[40:41], s[22:23], v34, s4, v[32:33]
	v_or_b32_e32 v7, 7, v7
	v_mad_i64_i32 v[42:43], s[22:23], v7, s4, v[32:33]
	global_load_dwordx4 v[32:35], v[40:41], off nt
	global_load_dwordx4 v[36:39], v[42:43], off nt
	s_waitcnt vmcnt(6)
	v_max3_f32 v7, |v8|, 0, |v12|
	v_max3_f32 v8, |v9|, 0, |v13|
	v_max3_f32 v9, |v10|, 0, |v14|
	v_max3_f32 v10, |v11|, 0, |v15|
	s_waitcnt vmcnt(4)
	v_max3_f32 v7, v7, |v16|, |v20|
	v_max3_f32 v8, v8, |v17|, |v21|
	v_max3_f32 v9, v9, |v18|, |v22|
	v_max3_f32 v10, v10, |v19|, |v23|
	s_waitcnt vmcnt(2)
	v_max3_f32 v7, v7, |v24|, |v28|
	v_max3_f32 v8, v8, |v25|, |v29|
	v_max3_f32 v11, v9, |v26|, |v30|
	v_max3_f32 v12, v10, |v27|, |v31|
	s_waitcnt vmcnt(0)
	v_max3_f32 v10, v7, |v32|, |v36|
	v_max3_f32 v9, v8, |v33|, |v37|
	v_max3_f32 v8, v11, |v34|, |v38|
	v_max3_f32 v7, v12, |v35|, |v39|

.LBB0_19:
	s_ashr_i32 s1, s0, 31
	s_lshr_b32 s1, s1, 24
	s_add_i32 s1, s0, s1
	s_ashr_i32 s4, s1, 8
	s_and_b32 s1, s1, 0xff00
	s_sub_i32 s1, s0, s1
	s_sext_i32_i16 s3, s1
	s_bfe_u32 s3, s3, 0x5001a
	s_add_i32 s3, s1, s3
	s_waitcnt lgkmcnt(0)
	s_sext_i32_i16 s8, s3
	s_and_b32 s3, s3, 0xffe0
	s_ashr_i32 s5, s4, 31
	s_lshl_b32 s8, s8, 3
	s_sub_i32 s1, s1, s3
	s_lshl_b64 s[4:5], s[4:5], 24
	s_and_b32 s3, s8, 0xffffff00
	s_sext_i32_i16 s1, s1
	s_add_u32 s4, s16, s4
	v_lshl_or_b32 v38, s1, 6, v3
	v_or_b32_e32 v40, s3, v4
	s_addc_u32 s5, s17, s5
	v_ashrrev_i32_e32 v39, 31, v38
	v_ashrrev_i32_e32 v41, 31, v40
	v_or_b32_e32 v6, 1, v40
	v_or_b32_e32 v8, 2, v40
	v_or_b32_e32 v10, 3, v40
	v_or_b32_e32 v12, 4, v40
	v_or_b32_e32 v14, 5, v40
	v_or_b32_e32 v16, 6, v40
	v_or_b32_e32 v18, 7, v40
	v_lshl_add_u64 v[20:21], v[38:39], 2, s[4:5]
	v_lshlrev_b64 v[22:23], 13, v[40:41]
	v_ashrrev_i32_e32 v7, 31, v6
	v_ashrrev_i32_e32 v9, 31, v8
	v_ashrrev_i32_e32 v11, 31, v10
	v_ashrrev_i32_e32 v13, 31, v12
	v_ashrrev_i32_e32 v15, 31, v14
	v_ashrrev_i32_e32 v17, 31, v16
	v_ashrrev_i32_e32 v19, 31, v18
	v_lshl_add_u64 v[42:43], v[20:21], 0, v[22:23]
	v_lshlrev_b64 v[6:7], 13, v[6:7]
	v_lshlrev_b64 v[8:9], 13, v[8:9]
	v_lshlrev_b64 v[10:11], 13, v[10:11]
	v_lshlrev_b64 v[12:13], 13, v[12:13]
	v_lshlrev_b64 v[14:15], 13, v[14:15]
	v_lshlrev_b64 v[16:17], 13, v[16:17]
	v_lshlrev_b64 v[18:19], 13, v[18:19]
	v_lshl_add_u64 v[44:45], v[20:21], 0, v[6:7]
	v_lshl_add_u64 v[46:47], v[20:21], 0, v[8:9]
	v_lshl_add_u64 v[48:49], v[20:21], 0, v[10:11]
	v_lshl_add_u64 v[50:51], v[20:21], 0, v[12:13]
	v_lshl_add_u64 v[52:53], v[20:21], 0, v[14:15]
	v_lshl_add_u64 v[54:55], v[20:21], 0, v[16:17]
	v_lshl_add_u64 v[56:57], v[20:21], 0, v[18:19]
	global_load_dwordx4 v[6:9], v[42:43], off nt
	global_load_dwordx4 v[10:13], v[44:45], off nt
	global_load_dwordx4 v[14:17], v[46:47], off nt
	global_load_dwordx4 v[18:21], v[48:49], off nt
	global_load_dwordx4 v[22:25], v[50:51], off nt
	global_load_dwordx4 v[26:29], v[52:53], off nt
	global_load_dwordx4 v[30:33], v[54:55], off nt
	global_load_dwordx4 v[34:37], v[56:57], off nt
	v_or_b32_e32 v42, 1, v38
	v_or_b32_e32 v44, 2, v38
	v_or_b32_e32 v46, 3, v38
	v_lshlrev_b64 v[38:39], 12, v[38:39]
	v_ashrrev_i32_e32 v43, 31, v42
	v_ashrrev_i32_e32 v45, 31, v44
	v_ashrrev_i32_e32 v47, 31, v46
	v_lshlrev_b64 v[40:41], 1, v[40:41]
	v_lshl_add_u64 v[38:39], s[18:19], 0, v[38:39]
	v_lshlrev_b64 v[42:43], 12, v[42:43]
	v_lshlrev_b64 v[44:45], 12, v[44:45]
	v_lshlrev_b64 v[46:47], 12, v[46:47]
	v_lshl_add_u64 v[48:49], v[38:39], 0, v[40:41]
	v_lshl_add_u64 v[38:39], s[18:19], 0, v[42:43]
	v_lshl_add_u64 v[42:43], s[18:19], 0, v[44:45]
	v_lshl_add_u64 v[44:45], s[18:19], 0, v[46:47]
	v_lshl_add_u64 v[46:47], v[38:39], 0, v[40:41]
	v_lshl_add_u64 v[42:43], v[42:43], 0, v[40:41]
	v_lshl_add_u64 v[44:45], v[44:45], 0, v[40:41]
	s_waitcnt vmcnt(6)
	v_cvt_pk_bf16_f32 v38, v6, v10
	s_waitcnt vmcnt(4)
	v_cvt_pk_bf16_f32 v39, v14, v18
	s_waitcnt vmcnt(2)
	v_cvt_pk_bf16_f32 v40, v22, v26
	s_waitcnt vmcnt(0)
	v_cvt_pk_bf16_f32 v41, v30, v34
	global_store_dwordx4 v[48:49], v[38:41], off
	s_nop 1
	v_cvt_pk_bf16_f32 v38, v7, v11
	v_cvt_pk_bf16_f32 v39, v15, v19
	v_cvt_pk_bf16_f32 v40, v23, v27
	v_cvt_pk_bf16_f32 v41, v31, v35
	global_store_dwordx4 v[46:47], v[38:41], off
	s_nop 1
	v_cvt_pk_bf16_f32 v38, v8, v12
	v_cvt_pk_bf16_f32 v39, v16, v20
	v_cvt_pk_bf16_f32 v40, v24, v28
	v_cvt_pk_bf16_f32 v41, v32, v36
	global_store_dwordx4 v[42:43], v[38:41], off
	v_cvt_pk_bf16_f32 v6, v9, v13
	v_cvt_pk_bf16_f32 v7, v17, v21
	v_cvt_pk_bf16_f32 v8, v25, v29
	v_cvt_pk_bf16_f32 v9, v33, v37
	global_store_dwordx4 v[44:45], v[6:9], off
	s_load_dword s1, s[6:7], 0x0
	s_waitcnt lgkmcnt(0)
	s_add_i32 s0, s1, s0
	s_cmpk_lt_i32 s0, 0x100
	s_cbranch_scc1 .LBB0_19

.LBB0_22:
	s_ashr_i32 s1, s0, 31
	s_lshr_b32 s1, s1, 29
	s_add_i32 s1, s0, s1
	s_ashr_i32 s4, s1, 3
	s_and_b32 s1, s1, 0xfffff8
	s_sub_i32 s1, s0, s1
	s_ashr_i32 s5, s4, 31
	v_lshl_or_b32 v44, s1, 8, v1
	s_lshl_b64 s[4:5], s[4:5], 19
	v_ashrrev_i32_e32 v45, 31, v44
	v_or_b32_e32 v14, 1, v44
	v_or_b32_e32 v16, 2, v44
	v_or_b32_e32 v18, 3, v44
	v_or_b32_e32 v20, 4, v44
	v_or_b32_e32 v22, 5, v44
	v_or_b32_e32 v24, 6, v44
	v_or_b32_e32 v26, 7, v44
	v_lshl_add_u64 v[12:13], v[2:3], 0, s[4:5]
	v_lshlrev_b64 v[28:29], 8, v[44:45]
	v_ashrrev_i32_e32 v15, 31, v14
	v_ashrrev_i32_e32 v17, 31, v16
	v_ashrrev_i32_e32 v19, 31, v18
	v_ashrrev_i32_e32 v21, 31, v20
	v_ashrrev_i32_e32 v23, 31, v22
	v_ashrrev_i32_e32 v25, 31, v24
	v_ashrrev_i32_e32 v27, 31, v26
	v_lshl_add_u64 v[46:47], v[12:13], 0, v[28:29]
	v_lshlrev_b64 v[14:15], 8, v[14:15]
	v_lshlrev_b64 v[16:17], 8, v[16:17]
	v_lshlrev_b64 v[18:19], 8, v[18:19]
	v_lshlrev_b64 v[20:21], 8, v[20:21]
	v_lshlrev_b64 v[22:23], 8, v[22:23]
	v_lshlrev_b64 v[24:25], 8, v[24:25]
	v_lshlrev_b64 v[26:27], 8, v[26:27]
	v_lshl_add_u64 v[48:49], v[12:13], 0, v[14:15]
	v_lshl_add_u64 v[50:51], v[12:13], 0, v[16:17]
	v_lshl_add_u64 v[52:53], v[12:13], 0, v[18:19]
	v_lshl_add_u64 v[54:55], v[12:13], 0, v[20:21]
	v_lshl_add_u64 v[56:57], v[12:13], 0, v[22:23]
	v_lshl_add_u64 v[58:59], v[12:13], 0, v[24:25]
	v_lshl_add_u64 v[60:61], v[12:13], 0, v[26:27]
	global_load_dwordx4 v[12:15], v[46:47], off nt
	global_load_dwordx4 v[16:19], v[48:49], off nt
	global_load_dwordx4 v[20:23], v[50:51], off nt
	global_load_dwordx4 v[24:27], v[52:53], off nt
	global_load_dwordx4 v[28:31], v[54:55], off nt
	global_load_dwordx4 v[32:35], v[56:57], off nt
	global_load_dwordx4 v[36:39], v[58:59], off nt
	global_load_dwordx4 v[40:43], v[60:61], off nt
	v_lshlrev_b64 v[44:45], 1, v[44:45]
	v_lshl_add_u64 v[48:49], v[4:5], 0, v[44:45]
	v_lshl_add_u64 v[50:51], v[6:7], 0, v[44:45]
	v_lshl_add_u64 v[52:53], v[8:9], 0, v[44:45]
	v_lshl_add_u64 v[54:55], v[10:11], 0, v[44:45]
	s_waitcnt vmcnt(6)
	v_cvt_pk_bf16_f32 v44, v12, v16
	s_waitcnt vmcnt(4)
	v_cvt_pk_bf16_f32 v45, v20, v24
	s_waitcnt vmcnt(2)
	v_cvt_pk_bf16_f32 v46, v28, v32
	s_waitcnt vmcnt(0)
	v_cvt_pk_bf16_f32 v47, v36, v40
	global_store_dwordx4 v[48:49], v[44:47], off
	s_nop 1
	v_cvt_pk_bf16_f32 v44, v13, v17
	v_cvt_pk_bf16_f32 v45, v21, v25
	v_cvt_pk_bf16_f32 v46, v29, v33
	v_cvt_pk_bf16_f32 v47, v37, v41
	global_store_dwordx4 v[50:51], v[44:47], off
	s_nop 1
	v_cvt_pk_bf16_f32 v44, v14, v18
	v_cvt_pk_bf16_f32 v45, v22, v26
	v_cvt_pk_bf16_f32 v46, v30, v34
	v_cvt_pk_bf16_f32 v47, v38, v42
	global_store_dwordx4 v[52:53], v[44:47], off
	v_cvt_pk_bf16_f32 v12, v15, v19
	v_cvt_pk_bf16_f32 v13, v23, v27
	v_cvt_pk_bf16_f32 v14, v31, v35
	v_cvt_pk_bf16_f32 v15, v39, v43
	global_store_dwordx4 v[54:55], v[12:15], off
	s_load_dword s1, s[6:7], 0x0
	s_waitcnt lgkmcnt(0)
	s_add_i32 s0, s1, s0
	s_cmp_gt_i32 s0, 7
	s_cbranch_scc0 .LBB0_22
